# stick-breaking attention: K loads older than V loads (setup de-interleaved); K staging ladder waits only for K (vmcnt 15..8), V staging has its own mid-tile ladder; on top of d3
# speedup vs baseline: 1.0018x; 1.0018x over previous
.LBB0_452:
	s_or_b64 exec, exec, s[10:11]
	v_readfirstlane_b32 s10, v0
	s_cmpk_gt_i32 s10, 0x7ff
	s_cselect_b64 s[30:31], -1, 0
	s_and_b64 vcc, exec, s[30:31]
	s_cbranch_vccnz .LBB0_447
	s_lshl_b32 s14, s10, 1
	s_and_b32 s47, s10, 0x780
	s_lshl_b32 s11, s10, 5
	s_add_i32 s10, s14, s46
	s_and_b32 s56, s11, 0xfe0
	s_and_b32 s57, s10, 0xfffff000
	s_or_b32 s15, s57, s56
	s_lshl_b32 s10, s47, 1
	s_add_u32 s10, s50, s10
	s_addc_u32 s11, s51, 0
	v_add_u32_e32 v32, s15, v174
	v_mov_b64_e32 v[24:25], s[10:11]
	v_add_u32_e32 v34, s15, v175
	v_add_u32_e32 v36, s15, v176
	v_add_u32_e32 v38, s15, v177
	v_add_u32_e32 v40, s15, v178
	v_add_u32_e32 v41, s15, v179
	v_mad_i64_i32 v[0:1], s[12:13], v32, s3, v[24:25]
	v_mad_i64_i32 v[2:3], s[12:13], v34, s3, v[24:25]
	v_mad_i64_i32 v[8:9], s[12:13], v36, s3, v[24:25]
	v_mad_i64_i32 v[10:11], s[12:13], v38, s3, v[24:25]
	v_mad_i64_i32 v[16:17], s[12:13], v40, s3, v[24:25]
	v_mad_i64_i32 v[18:19], s[12:13], v41, s3, v[24:25]
	v_lshl_add_u64 v[0:1], v[0:1], 0, v[160:161]
	v_lshl_add_u64 v[4:5], v[2:3], 0, v[160:161]
	v_lshl_add_u64 v[8:9], v[8:9], 0, v[160:161]
	v_lshl_add_u64 v[12:13], v[10:11], 0, v[160:161]
	v_lshl_add_u64 v[16:17], v[16:17], 0, v[160:161]
	v_lshl_add_u64 v[20:21], v[18:19], 0, v[160:161]
	global_load_dwordx4 v[0:3], v[0:1], off
	s_nop 0
	global_load_dwordx4 v[4:7], v[4:5], off
	s_nop 0
	global_load_dwordx4 v[8:11], v[8:9], off
	s_nop 0
	global_load_dwordx4 v[12:15], v[12:13], off
	s_nop 0
	global_load_dwordx4 v[16:19], v[16:17], off
	s_nop 0
	global_load_dwordx4 v[20:23], v[20:21], off
	v_mov_b32_e32 v147, v161
	v_lshl_add_u64 v[148:149], s[10:11], 0, v[146:147]
	s_mov_b64 s[98:99], 0x2000
	v_lshl_add_u64 v[216:217], v[148:149], 0, s[98:99]
	v_mad_i64_i32 v[32:33], s[10:11], v32, s3, v[148:149]
	v_add_co_u32_e32 v32, vcc, s93, v32
	v_mad_i64_i32 v[34:35], s[10:11], v34, s3, v[148:149]
	s_nop 0
	v_addc_co_u32_e32 v33, vcc, 0, v33, vcc
	v_add_co_u32_e32 v34, vcc, s93, v34
	v_mad_i64_i32 v[36:37], s[10:11], v36, s3, v[148:149]
	s_nop 0
	v_addc_co_u32_e32 v35, vcc, 0, v35, vcc
	v_add_u32_e32 v42, s15, v180
	v_add_u32_e32 v43, s15, v181
	v_add_co_u32_e32 v36, vcc, s93, v36
	v_mad_i64_i32 v[26:27], s[12:13], v42, s3, v[24:25]
	v_mad_i64_i32 v[24:25], s[12:13], v43, s3, v[24:25]
	v_mad_i64_i32 v[38:39], s[10:11], v38, s3, v[148:149]
	v_addc_co_u32_e32 v37, vcc, 0, v37, vcc
	v_lshl_add_u64 v[26:27], v[26:27], 0, v[160:161]
	v_lshl_add_u64 v[28:29], v[24:25], 0, v[160:161]
	v_add_co_u32_e32 v38, vcc, s93, v38
	global_load_dwordx4 v[24:27], v[26:27], off
	s_nop 0
	global_load_dwordx4 v[28:31], v[28:29], off
	v_addc_co_u32_e32 v39, vcc, 0, v39, vcc
	v_mad_i64_i32 v[44:45], s[10:11], v40, s3, v[216:217]
	v_mad_i64_i32 v[46:47], s[10:11], v41, s3, v[216:217]
	v_mad_i64_i32 v[50:51], s[10:11], v42, s3, v[216:217]
	v_mad_i64_i32 v[52:53], s[10:11], v43, s3, v[216:217]
	global_load_dwordx4 v[80:83], v[32:33], off offset:-4096
	global_load_dwordx4 v[88:91], v[34:35], off offset:-4096
	global_load_dwordx4 v[96:99], v[36:37], off offset:-4096
	global_load_dwordx4 v[104:107], v[38:39], off offset:-4096
	global_load_dwordx4 v[112:115], v[44:45], off offset:-4096
	global_load_dwordx4 v[120:123], v[46:47], off offset:-4096
	global_load_dwordx4 v[128:131], v[50:51], off offset:-4096
	global_load_dwordx4 v[136:139], v[52:53], off offset:-4096
	global_load_dwordx4 v[84:87], v[32:33], off
	global_load_dwordx4 v[92:95], v[34:35], off
	global_load_dwordx4 v[100:103], v[36:37], off
	global_load_dwordx4 v[108:111], v[38:39], off
	global_load_dwordx4 v[116:119], v[44:45], off
	global_load_dwordx4 v[124:127], v[46:47], off
	global_load_dwordx4 v[132:135], v[50:51], off
	global_load_dwordx4 v[140:143], v[52:53], off
	v_mov_b32_e32 v48, 0
	s_mov_b32 s58, 0
	v_mov_b32_e32 v205, 1.0
	v_mov_b32_e32 v49, v48
	v_mov_b32_e32 v50, v48
	v_mov_b32_e32 v51, v48
	v_mov_b32_e32 v52, v48
	v_mov_b32_e32 v53, v48
	v_mov_b32_e32 v54, v48
	v_mov_b32_e32 v55, v48
	v_mov_b32_e32 v56, v48
	v_mov_b32_e32 v57, v48
	v_mov_b32_e32 v58, v48
	v_mov_b32_e32 v59, v48
	v_mov_b32_e32 v60, v48
	v_mov_b32_e32 v61, v48
	v_mov_b32_e32 v62, v48
	s_add_i32 s10, s43, s14
	s_and_b32 s10, s10, 0xfffff000
	s_or_b32 s10, s56, s10
	s_waitcnt vmcnt(16)
	ds_write_b128 v190, v[0:3] offset:8192
	ds_write_b128 v191, v[4:7] offset:8192
	ds_write_b128 v192, v[8:11] offset:8192
	ds_write_b128 v193, v[12:15] offset:8192
	ds_write_b128 v194, v[16:19] offset:8192
	ds_write_b128 v195, v[20:23] offset:8192
	ds_write_b128 v196, v[24:27] offset:8192
	ds_write_b128 v197, v[28:31] offset:8192
	v_add_u32_e32 v147, s10, v182
	v_add_u32_e32 v198, s10, v183
	v_add_u32_e32 v199, s10, v184
	v_add_u32_e32 v200, s10, v185
	v_add_u32_e32 v201, s10, v186
	v_add_u32_e32 v202, s10, v187
	v_add_u32_e32 v203, s10, v188
	v_add_u32_e32 v204, s10, v189
	v_mov_b32_e32 v63, v48
	v_mov_b32_e32 v32, v48
	v_mov_b32_e32 v33, v48
	v_mov_b32_e32 v34, v48
	v_mov_b32_e32 v35, v48
	v_mov_b32_e32 v36, v48
	v_mov_b32_e32 v37, v48
	v_mov_b32_e32 v38, v48
	v_mov_b32_e32 v39, v48
	v_mov_b32_e32 v40, v48
	v_mov_b32_e32 v41, v48
	v_mov_b32_e32 v42, v48
	v_mov_b32_e32 v43, v48
	v_mov_b32_e32 v44, v48
	v_mov_b32_e32 v45, v48
	v_mov_b32_e32 v46, v48
	v_mov_b32_e32 v47, v48
	v_mov_b32_e32 v16, v48
	v_mov_b32_e32 v17, v48
	v_mov_b32_e32 v18, v48
	v_mov_b32_e32 v19, v48
	v_mov_b32_e32 v20, v48
	v_mov_b32_e32 v21, v48
	v_mov_b32_e32 v22, v48
	v_mov_b32_e32 v23, v48
	v_mov_b32_e32 v24, v48
	v_mov_b32_e32 v25, v48
	v_mov_b32_e32 v26, v48
	v_mov_b32_e32 v27, v48
	v_mov_b32_e32 v28, v48
	v_mov_b32_e32 v29, v48
	v_mov_b32_e32 v30, v48
	v_mov_b32_e32 v31, v48
	v_mov_b32_e32 v0, v48
	v_mov_b32_e32 v1, v48
	v_mov_b32_e32 v2, v48
	v_mov_b32_e32 v3, v48
	v_mov_b32_e32 v4, v48
	v_mov_b32_e32 v5, v48
	v_mov_b32_e32 v6, v48
	v_mov_b32_e32 v7, v48
	v_mov_b32_e32 v8, v48
	v_mov_b32_e32 v9, v48
	v_mov_b32_e32 v10, v48
	v_mov_b32_e32 v11, v48
	v_mov_b32_e32 v12, v48
	v_mov_b32_e32 v13, v48
	v_mov_b32_e32 v14, v48
	v_mov_b32_e32 v15, v48
	s_branch .LBB0_455

.LBB0_455:
	v_mov_b32_e32 v206, v172
	s_cmp_lg_u32 s58, 0
	v_lshrrev_b32_e32 v64, 4, v206
	v_lshlrev_b32_e32 v66, 4, v206
	v_lshlrev_b32_e32 v65, 8, v64
	v_lshlrev_b32_e32 v64, 6, v64
	v_and_b32_e32 v66, 0xf0, v66
	v_xad_u32 v64, v64, v66, v65
	v_lshlrev_b32_e32 v65, 2, v206
	v_and_b32_e32 v168, 31, v206
	v_ashrrev_i32_e32 v169, 5, v206
	v_and_b32_e32 v65, 12, v65
	v_bfe_u32 v207, v206, 2, 2
	v_bitop3_b32 v65, v65, v169, v207 bitop3:0x36
	v_add_u32_e32 v158, s42, v64
	v_xad_u32 v159, v64, 16, s42
	v_xad_u32 v162, v64, 32, s42
	v_xad_u32 v163, v64, 48, s42
	v_lshlrev_b32_e32 v64, 8, v168
	v_lshl_add_u32 v166, v65, 4, v64
	s_waitcnt vmcnt(15)
	ds_write_b128 v158, v[80:83]
	s_waitcnt vmcnt(14)
	ds_write_b128 v159, v[88:91] offset:1024
	s_waitcnt vmcnt(13)
	ds_write_b128 v162, v[96:99] offset:2048
	s_waitcnt vmcnt(12)
	ds_write_b128 v163, v[104:107] offset:3072
	s_waitcnt vmcnt(11)
	ds_write_b128 v158, v[112:115] offset:4096
	s_waitcnt vmcnt(10)
	ds_write_b128 v159, v[120:123] offset:5120
	s_waitcnt vmcnt(9)
	ds_write_b128 v162, v[128:131] offset:6144
	s_waitcnt vmcnt(8)
	ds_write_b128 v163, v[136:139] offset:7168
	v_add_u32_e32 v218, s58, v204
	v_mad_i64_i32 v[80:81], s[98:99], v218, s3, v[216:217]
	global_load_dwordx4 v[80:83], v[80:81], off offset:-4096
	v_add_u32_e32 v218, s58, v203
	v_mad_i64_i32 v[88:89], s[98:99], v218, s3, v[216:217]
	global_load_dwordx4 v[88:91], v[88:89], off offset:-4096
	v_add_u32_e32 v218, s58, v202
	v_mad_i64_i32 v[96:97], s[98:99], v218, s3, v[216:217]
	global_load_dwordx4 v[96:99], v[96:97], off offset:-4096
	v_add_u32_e32 v218, s58, v201
	v_mad_i64_i32 v[104:105], s[98:99], v218, s3, v[216:217]
	global_load_dwordx4 v[104:107], v[104:105], off offset:-4096
	v_add_u32_e32 v218, s58, v200
	v_mad_i64_i32 v[112:113], s[98:99], v218, s3, v[216:217]
	global_load_dwordx4 v[112:115], v[112:113], off offset:-4096
	v_add_u32_e32 v218, s58, v199
	v_mad_i64_i32 v[120:121], s[98:99], v218, s3, v[216:217]
	global_load_dwordx4 v[120:123], v[120:121], off offset:-4096
	v_add_u32_e32 v218, s58, v198
	v_mad_i64_i32 v[128:129], s[98:99], v218, s3, v[216:217]
	global_load_dwordx4 v[128:131], v[128:129], off offset:-4096
	v_add_u32_e32 v218, s58, v147
	v_mad_i64_i32 v[136:137], s[98:99], v218, s3, v[216:217]
	global_load_dwordx4 v[136:139], v[136:137], off offset:-4096
	v_add_u32_e32 v68, s42, v166
	ds_read_b128 v[64:67], v68
	ds_read_b128 v[68:71], v68 offset:8192
	s_waitcnt lgkmcnt(0)
	v_mfma_f32_32x32x16_bf16 v[64:79], v[64:67], v[68:71], 0
	v_xad_u32 v154, v166, 32, s42
	ds_read_b128 v[150:153], v154
	ds_read_b128 v[154:157], v154 offset:8192
	v_xad_u32 v167, v166, 64, s42
	s_waitcnt lgkmcnt(0)
	v_mfma_f32_32x32x16_bf16 v[64:79], v[150:153], v[154:157], v[64:79]
	ds_read_b128 v[150:153], v167
	ds_read_b128 v[154:157], v167 offset:8192
	v_xor_b32_e32 v167, 0x60, v166
	v_add_u32_e32 v167, s42, v167
	s_waitcnt lgkmcnt(0)
	v_mfma_f32_32x32x16_bf16 v[64:79], v[150:153], v[154:157], v[64:79]
	ds_read_b128 v[150:153], v167
	ds_read_b128 v[154:157], v167 offset:8192
	v_xor_b32_e32 v167, 0x80, v166
	v_add_u32_e32 v167, s42, v167
	s_waitcnt lgkmcnt(0)
	v_mfma_f32_32x32x16_bf16 v[64:79], v[150:153], v[154:157], v[64:79]
	ds_read_b128 v[150:153], v167
	ds_read_b128 v[154:157], v167 offset:8192
	v_xor_b32_e32 v167, 0xa0, v166
	v_add_u32_e32 v167, s42, v167
	s_waitcnt lgkmcnt(0)
	v_mfma_f32_32x32x16_bf16 v[64:79], v[150:153], v[154:157], v[64:79]
	ds_read_b128 v[150:153], v167
	ds_read_b128 v[154:157], v167 offset:8192
	v_xor_b32_e32 v167, 0xc0, v166
	v_add_u32_e32 v167, s42, v167
	ds_read_b128 v[208:211], v167
	s_waitcnt lgkmcnt(1)
	v_mfma_f32_32x32x16_bf16 v[64:79], v[150:153], v[154:157], v[64:79]
	ds_read_b128 v[150:153], v167 offset:8192
	v_xor_b32_e32 v154, 0xe0, v166
	v_add_u32_e32 v166, s42, v154
	ds_read_b128 v[154:157], v166
	ds_read_b128 v[212:215], v166 offset:8192
	s_waitcnt lgkmcnt(0)
	s_waitcnt vmcnt(15)
	ds_write_b128 v158, v[84:87]
	s_waitcnt vmcnt(14)
	ds_write_b128 v159, v[92:95] offset:1024
	s_waitcnt vmcnt(13)
	ds_write_b128 v162, v[100:103] offset:2048
	s_waitcnt vmcnt(12)
	ds_write_b128 v163, v[108:111] offset:3072
	s_waitcnt vmcnt(11)
	ds_write_b128 v158, v[116:119] offset:4096
	s_waitcnt vmcnt(10)
	ds_write_b128 v159, v[124:127] offset:5120
	s_waitcnt vmcnt(9)
	ds_write_b128 v162, v[132:135] offset:6144
	s_waitcnt vmcnt(8)
	ds_write_b128 v163, v[140:143] offset:7168
	v_add_u32_e32 v218, s58, v204
	v_mad_i64_i32 v[84:85], s[98:99], v218, s3, v[216:217]
	global_load_dwordx4 v[84:87], v[84:85], off
	v_add_u32_e32 v218, s58, v203
	v_mad_i64_i32 v[92:93], s[98:99], v218, s3, v[216:217]
	global_load_dwordx4 v[92:95], v[92:93], off
	v_add_u32_e32 v218, s58, v202
	v_mad_i64_i32 v[100:101], s[98:99], v218, s3, v[216:217]
	global_load_dwordx4 v[100:103], v[100:101], off
	v_add_u32_e32 v218, s58, v201
	v_mad_i64_i32 v[108:109], s[98:99], v218, s3, v[216:217]
	global_load_dwordx4 v[108:111], v[108:109], off
	v_add_u32_e32 v218, s58, v200
	v_mad_i64_i32 v[116:117], s[98:99], v218, s3, v[216:217]
	global_load_dwordx4 v[116:119], v[116:117], off
	v_add_u32_e32 v218, s58, v199
	v_mad_i64_i32 v[124:125], s[98:99], v218, s3, v[216:217]
	global_load_dwordx4 v[124:127], v[124:125], off
	v_add_u32_e32 v218, s58, v198
	v_mad_i64_i32 v[132:133], s[98:99], v218, s3, v[216:217]
	global_load_dwordx4 v[132:135], v[132:133], off
	v_add_u32_e32 v218, s58, v147
	v_mad_i64_i32 v[140:141], s[98:99], v218, s3, v[216:217]
	global_load_dwordx4 v[140:143], v[140:141], off
	s_waitcnt lgkmcnt(10)
	v_mfma_f32_32x32x16_bf16 v[64:79], v[208:211], v[150:153], v[64:79]
	s_waitcnt lgkmcnt(8)
	v_mfma_f32_32x32x16_bf16 v[64:79], v[154:157], v[212:215], v[64:79]
	s_nop 11
	v_mul_f32_e32 v64, 0x3db504f3, v64
	v_mul_f32_e32 v65, 0x3db504f3, v65
	v_min_f32_e32 v64, 0x42a00000, v64
	v_min_f32_e32 v65, 0x42a00000, v65
	v_mul_f32_e32 v67, 0x3db504f3, v67
	v_mul_f32_e32 v64, 0x3fb8aa3b, v64
	v_mul_f32_e32 v65, 0x3fb8aa3b, v65
	v_min_f32_e32 v67, 0x42a00000, v67
	v_exp_f32_e32 v64, v64
	v_exp_f32_e32 v65, v65
	v_mul_f32_e32 v67, 0x3fb8aa3b, v67
	v_exp_f32_e32 v152, v67
	v_mul_f32_e32 v67, 0x3db504f3, v68
	v_min_f32_e32 v67, 0x42a00000, v67
	v_mul_f32_e32 v67, 0x3fb8aa3b, v67
	v_add_f32_e32 v150, 1.0, v64
	v_add_f32_e32 v151, 1.0, v65
	v_exp_f32_e32 v68, v67
	v_mul_f32_e32 v67, 0x3db504f3, v69
	v_rcp_f32_e32 v154, v150
	v_rcp_f32_e32 v155, v151
	v_min_f32_e32 v67, 0x42a00000, v67
	v_mul_f32_e32 v67, 0x3fb8aa3b, v67
	v_exp_f32_e32 v69, v67
	v_pk_mul_f32 v[150:151], v[64:65], v[154:155]
	v_add_f32_e32 v65, 1.0, v152
	v_rcp_f32_e32 v67, v65
	v_add_f32_e32 v65, 1.0, v68
	v_rcp_f32_e32 v156, v65
	v_add_f32_e32 v65, 1.0, v69
	v_mul_f32_e32 v66, 0x3db504f3, v66
	v_rcp_f32_e32 v157, v65
	v_min_f32_e32 v66, 0x42a00000, v66
	v_mul_f32_e32 v66, 0x3fb8aa3b, v66
	v_exp_f32_e32 v66, v66
	v_mul_f32_e32 v210, v152, v67
	v_pk_mul_f32 v[152:153], v[68:69], v[156:157]
	v_mul_f32_e32 v68, 0x3db504f3, v71
	v_mul_f32_e32 v65, 0x3db504f3, v70
	v_min_f32_e32 v68, 0x42a00000, v68
	v_min_f32_e32 v65, 0x42a00000, v65
	v_mul_f32_e32 v68, 0x3fb8aa3b, v68
	v_add_f32_e32 v64, 1.0, v66
	v_mul_f32_e32 v65, 0x3fb8aa3b, v65
	v_exp_f32_e32 v162, v68
	v_mul_f32_e32 v68, 0x3db504f3, v72
	v_rcp_f32_e32 v64, v64
	v_exp_f32_e32 v65, v65
	v_min_f32_e32 v68, 0x42a00000, v68
	v_mul_f32_e32 v68, 0x3fb8aa3b, v68
	v_exp_f32_e32 v70, v68
	v_mul_f32_e32 v68, 0x3db504f3, v73
	v_min_f32_e32 v68, 0x42a00000, v68
	v_mul_f32_e32 v211, v66, v64
	v_add_f32_e32 v66, 1.0, v65
	v_mul_f32_e32 v68, 0x3fb8aa3b, v68
	v_rcp_f32_e32 v66, v66
	v_exp_f32_e32 v71, v68
	v_mul_f32_e32 v68, 0x3db504f3, v74
	v_min_f32_e32 v68, 0x42a00000, v68
	v_mul_f32_e32 v68, 0x3fb8aa3b, v68
	v_exp_f32_e32 v72, v68
	v_mul_f32_e32 v212, v65, v66
	v_add_f32_e32 v65, 1.0, v162
	v_rcp_f32_e32 v69, v65
	v_add_f32_e32 v65, 1.0, v70
	v_rcp_f32_e32 v158, v65
	v_add_f32_e32 v65, 1.0, v71
	v_rcp_f32_e32 v159, v65
	v_add_f32_e32 v65, 1.0, v72
	v_rcp_f32_e32 v68, v65
	v_mul_f32_e32 v65, 0x3db504f3, v75
	v_min_f32_e32 v65, 0x42a00000, v65
	v_mul_f32_e32 v65, 0x3fb8aa3b, v65
	v_exp_f32_e32 v65, v65
	v_pk_mul_f32 v[74:75], v[70:71], v[158:159]
	v_mul_f32_e32 v213, v72, v68
	v_mul_f32_e32 v214, v162, v69
	v_add_f32_e32 v70, 1.0, v65
	v_rcp_f32_e32 v71, v70
	v_mul_f32_e32 v70, 0x3db504f3, v76
	v_min_f32_e32 v70, 0x42a00000, v70
	v_mul_f32_e32 v70, 0x3fb8aa3b, v70
	v_exp_f32_e32 v72, v70
	v_mul_f32_e32 v70, 0x3db504f3, v77
	v_min_f32_e32 v70, 0x42a00000, v70
	v_mul_f32_e32 v70, 0x3fb8aa3b, v70
	v_exp_f32_e32 v73, v70
	v_mul_f32_e32 v70, 0x3db504f3, v78
	v_min_f32_e32 v70, 0x42a00000, v70
	v_mul_f32_e32 v70, 0x3fb8aa3b, v70
	v_exp_f32_e32 v76, v70
	v_mul_f32_e32 v70, 0x3db504f3, v79
	v_min_f32_e32 v70, 0x42a00000, v70
	v_mul_f32_e32 v70, 0x3fb8aa3b, v70
	v_exp_f32_e32 v77, v70
	v_mul_f32_e32 v215, v65, v71
	v_add_f32_e32 v65, 1.0, v72
	v_rcp_f32_e32 v166, v65
	v_add_f32_e32 v65, 1.0, v73
	v_rcp_f32_e32 v167, v65
	v_add_f32_e32 v65, 1.0, v76
	v_rcp_f32_e32 v70, v65
	v_add_f32_e32 v65, 1.0, v77
	v_rcp_f32_e32 v65, v65
	v_pk_mul_f32 v[72:73], v[72:73], v[166:167]
	v_mul_f32_e32 v208, v76, v70
	v_mul_f32_e32 v209, v77, v65
	s_cbranch_scc1 .LBB0_457
	v_lshlrev_b32_e32 v76, 2, v169
	v_or_b32_e32 v77, 1, v76
	v_cmp_lt_i32_e32 vcc, v76, v168
	v_cmp_lt_i32_e64 s[10:11], v77, v168
	v_or_b32_e32 v77, 2, v76
	v_cndmask_b32_e32 v150, 0, v150, vcc
	s_or_b64 s[70:71], s[10:11], vcc
	v_cmp_lt_i32_e32 vcc, v77, v168
	v_or_b32_e32 v77, 3, v76
	v_cmp_lt_i32_e64 s[12:13], v77, v168
	v_add_u32_e32 v77, 8, v76
	v_cmp_lt_i32_e64 s[14:15], v77, v168
	v_add_u32_e32 v77, 10, v76
	v_add_u32_e32 v78, 9, v76
	v_cmp_lt_i32_e64 s[16:17], v77, v168
	v_add_u32_e32 v77, 11, v76
	v_cndmask_b32_e32 v211, 0, v211, vcc
	s_or_b64 s[72:73], s[12:13], vcc
	v_cmp_lt_i32_e32 vcc, v78, v168
	v_cmp_lt_i32_e64 s[18:19], v77, v168
	s_or_b64 s[20:21], vcc, s[14:15]
	v_cndmask_b32_e64 v212, 0, v212, s[16:17]
	s_or_b64 s[16:17], s[18:19], s[16:17]
	s_or_b64 s[20:21], s[20:21], s[16:17]
	v_cndmask_b32_e64 v156, 1.0, v156, s[20:21]
	s_or_b64 s[20:21], s[20:21], s[72:73]
	v_cndmask_b32_e64 v151, 0, v151, s[10:11]
	s_or_b64 s[10:11], s[20:21], s[10:11]
	v_cndmask_b32_e32 v153, 0, v153, vcc
	v_cndmask_b32_e64 v155, 1.0, v155, s[10:11]
	s_or_b64 s[10:11], s[20:21], s[70:71]
	s_or_b64 vcc, s[16:17], vcc
	v_cndmask_b32_e64 v154, 1.0, v154, s[10:11]
	s_or_b64 s[10:11], vcc, s[14:15]
	v_add_u32_e32 v77, 16, v76
	v_cndmask_b32_e32 v157, 1.0, v157, vcc
	s_or_b64 vcc, s[10:11], s[12:13]
	v_cmp_lt_i32_e64 s[10:11], v77, v168
	v_add_u32_e32 v77, 18, v76
	v_cndmask_b32_e64 v210, 0, v210, s[12:13]
	v_cmp_lt_i32_e64 s[12:13], v77, v168
	v_add_u32_e32 v77, 19, v76
	v_cndmask_b32_e64 v152, 0, v152, s[14:15]
	v_add_u32_e32 v78, 17, v76
	v_cmp_lt_i32_e64 s[14:15], v77, v168
	v_cndmask_b32_e32 v67, 1.0, v67, vcc
	v_cmp_lt_i32_e32 vcc, v78, v168
	v_cndmask_b32_e64 v213, 0, v213, s[12:13]
	s_or_b64 s[12:13], s[14:15], s[12:13]
	v_cndmask_b32_e32 v75, 0, v75, vcc
	s_or_b64 vcc, s[12:13], vcc
	v_add_u32_e32 v77, 24, v76
	v_cndmask_b32_e64 v74, 0, v74, s[10:11]
	v_cndmask_b32_e32 v159, 1.0, v159, vcc
	s_or_b64 vcc, vcc, s[10:11]
	v_add_u32_e32 v78, 25, v76
	v_cmp_lt_i32_e64 s[10:11], v77, v168
	v_add_u32_e32 v77, 26, v76
	v_add_u32_e32 v76, 27, v76
	v_cndmask_b32_e64 v215, 0, v215, s[14:15]
	v_cndmask_b32_e64 v68, 1.0, v68, s[12:13]
	v_cndmask_b32_e64 v71, 1.0, v71, s[14:15]
	v_cmp_lt_i32_e64 s[12:13], v77, v168
	v_cmp_lt_i32_e64 s[14:15], v76, v168
	v_cndmask_b32_e32 v158, 1.0, v158, vcc
	v_cmp_lt_i32_e32 vcc, v78, v168
	v_cndmask_b32_e64 v208, 0, v208, s[12:13]
	s_or_b64 s[12:13], s[14:15], s[12:13]
	v_cndmask_b32_e32 v73, 0, v73, vcc
	s_or_b64 vcc, s[12:13], vcc
	v_cndmask_b32_e32 v167, 1.0, v167, vcc
	s_or_b64 vcc, vcc, s[10:11]
	v_cndmask_b32_e64 v214, 0, v214, s[18:19]
	v_cndmask_b32_e64 v66, 1.0, v66, s[16:17]
	v_cndmask_b32_e64 v64, 1.0, v64, s[20:21]
	v_cndmask_b32_e64 v69, 1.0, v69, s[18:19]
	v_cndmask_b32_e64 v72, 0, v72, s[10:11]
	v_cndmask_b32_e64 v209, 0, v209, s[14:15]
	v_cndmask_b32_e64 v70, 1.0, v70, s[12:13]
	v_cndmask_b32_e32 v166, 1.0, v166, vcc
	v_cndmask_b32_e64 v65, 1.0, v65, s[14:15]
